# attention band loop: causal mask folded into the bias table (xtab = -inf for negative distances), explicit compare/select mask blocks of the band loop removed
# baseline (speedup 1.0000x reference)
.LBB0_256:
	v_and_b32_e32 v3, 0xffffff80, v1
	v_cmp_eq_u32_e32 vcc, s10, v3
	v_mov_b32_e32 v3, 0xff800000
	v_cmp_le_u32_e64 s[4:5], s10, v1
	s_nop 1
	v_cndmask_b32_e64 v3, v3, 0, s[4:5]
	s_and_saveexec_b64 s[4:5], vcc
	s_cbranch_execz .LBB0_255
	v_add_u32_e32 v3, s9, v2
	ds_read_b32 v3, v3 offset:3072
	s_branch .LBB0_255

.LBB0_288:
	s_add_i32 s75, s73, s87
	s_add_i32 s38, s75, 4
	s_cmp_lt_i32 s38, 0
.LBB0_290:
	s_cmp_lt_i32 s87, s72
	v_add_u32_e32 v247, v244, v245
	s_cbranch_scc1 .LBB0_292
	v_add_u32_e32 v166, 0x1ebfc, v247
	v_add_u32_e32 v168, 0x1eb7c, v247
	v_add_u32_e32 v174, 0x1ebf4, v247
	v_add_u32_e32 v176, 0x1eb74, v247
	ds_read2_b32 v[166:167], v166 offset1:1
	ds_read2_b32 v[168:169], v168 offset1:1
	ds_read2_b32 v[174:175], v174 offset1:1
	ds_read2_b32 v[176:177], v176 offset1:1
	s_waitcnt lgkmcnt(3)
	v_add_f32_e32 v114, v114, v167
	s_waitcnt lgkmcnt(2)
	v_add_f32_e32 v98, v98, v169
	v_add_f32_e32 v115, v115, v166
	v_add_f32_e32 v99, v99, v168
	s_waitcnt lgkmcnt(1)
	v_add_f32_e32 v116, v116, v175
	s_waitcnt lgkmcnt(0)
	v_add_f32_e32 v100, v100, v177
	v_add_f32_e32 v117, v117, v174
	v_add_f32_e32 v101, v101, v176
	v_add_u32_e32 v178, 0x1eb14, v247
	v_add_u32_e32 v166, 0x1ebdc, v247
	v_add_u32_e32 v168, 0x1eb5c, v247
	v_add_u32_e32 v174, 0x1ebd4, v247
	v_add_u32_e32 v176, 0x1eb54, v247
	ds_read2_b32 v[166:167], v166 offset1:1
	ds_read2_b32 v[168:169], v168 offset1:1
	ds_read2_b32 v[174:175], v174 offset1:1
	ds_read2_b32 v[176:177], v176 offset1:1
	s_waitcnt lgkmcnt(3)
	v_add_f32_e32 v118, v118, v167
	s_waitcnt lgkmcnt(2)
	v_add_f32_e32 v102, v102, v169
	v_add_f32_e32 v119, v119, v166
	v_add_f32_e32 v103, v103, v168
	s_waitcnt lgkmcnt(1)
	v_add_f32_e32 v120, v120, v175
	s_waitcnt lgkmcnt(0)
	v_add_f32_e32 v104, v104, v177
	v_add_f32_e32 v121, v121, v174
	v_add_f32_e32 v105, v105, v176
	s_nop 0
	v_add_u32_e32 v166, 0x1ebbc, v247
	v_add_u32_e32 v168, 0x1eb3c, v247
	v_add_u32_e32 v174, 0x1ebb4, v247
	v_add_u32_e32 v176, 0x1eb34, v247
	ds_read2_b32 v[166:167], v166 offset1:1
	ds_read2_b32 v[168:169], v168 offset1:1
	ds_read2_b32 v[174:175], v174 offset1:1
	ds_read2_b32 v[176:177], v176 offset1:1
	s_waitcnt lgkmcnt(3)
	v_add_f32_e32 v122, v122, v167
	s_waitcnt lgkmcnt(2)
	v_add_f32_e32 v106, v106, v169
	v_add_f32_e32 v123, v123, v166
	v_add_f32_e32 v107, v107, v168
	s_waitcnt lgkmcnt(1)
	v_add_f32_e32 v124, v124, v175
	s_waitcnt lgkmcnt(0)
	v_add_f32_e32 v108, v108, v177
	v_add_f32_e32 v125, v125, v174
	v_add_f32_e32 v109, v109, v176
	s_nop 0
	v_add_u32_e32 v166, 0x1eb9c, v247
	v_add_u32_e32 v168, 0x1eb1c, v247
	v_add_u32_e32 v174, 0x1eb94, v247
	ds_read2_b32 v[166:167], v166 offset1:1
	ds_read2_b32 v[168:169], v168 offset1:1
	ds_read2_b32 v[174:175], v174 offset1:1
	ds_read2_b32 v[176:177], v178 offset1:1
	s_waitcnt lgkmcnt(3)
	v_add_f32_e32 v126, v126, v167
	s_waitcnt lgkmcnt(2)
	v_add_f32_e32 v110, v110, v169
	v_add_f32_e32 v127, v127, v166
	v_add_f32_e32 v111, v111, v168
	s_waitcnt lgkmcnt(1)
	v_add_f32_e32 v128, v128, v175
	s_waitcnt lgkmcnt(0)
	v_add_f32_e32 v112, v112, v177
	v_add_f32_e32 v129, v129, v174
	v_add_f32_e32 v113, v113, v176
	s_nop 0

.LBB0_303:
	s_add_i32 s75, s75, 5
	s_cmp_lt_i32 s75, 0
.LBB0_305:
	s_add_i32 s0, s87, 1
	s_cmp_lt_i32 s0, s72
	s_cbranch_scc1 .LBB0_307
	v_add_u32_e32 v16, 0x1eafc, v247
	v_add_u32_e32 v222, 0x1ea7c, v247
	v_add_u32_e32 v224, 0x1eaf4, v247
	v_add_u32_e32 v250, 0x1ea74, v247
	ds_read2_b32 v[16:17], v16 offset1:1
	ds_read2_b32 v[222:223], v222 offset1:1
	ds_read2_b32 v[224:225], v224 offset1:1
	ds_read2_b32 v[250:251], v250 offset1:1
	s_waitcnt lgkmcnt(3)
	v_add_f32_e32 v114, v114, v17
	s_waitcnt lgkmcnt(2)
	v_add_f32_e32 v98, v98, v223
	v_add_f32_e32 v115, v115, v16
	v_add_f32_e32 v99, v99, v222
	s_waitcnt lgkmcnt(1)
	v_add_f32_e32 v116, v116, v225
	s_waitcnt lgkmcnt(0)
	v_add_f32_e32 v100, v100, v251
	v_add_f32_e32 v117, v117, v224
	v_add_f32_e32 v101, v101, v250
	v_add_u32_e32 v252, 0x1ea14, v247
	v_add_u32_e32 v16, 0x1eadc, v247
	v_add_u32_e32 v222, 0x1ea5c, v247
	v_add_u32_e32 v224, 0x1ead4, v247
	v_add_u32_e32 v250, 0x1ea54, v247
	ds_read2_b32 v[16:17], v16 offset1:1
	ds_read2_b32 v[222:223], v222 offset1:1
	ds_read2_b32 v[224:225], v224 offset1:1
	ds_read2_b32 v[250:251], v250 offset1:1
	s_waitcnt lgkmcnt(3)
	v_add_f32_e32 v118, v118, v17
	s_waitcnt lgkmcnt(2)
	v_add_f32_e32 v102, v102, v223
	v_add_f32_e32 v119, v119, v16
	v_add_f32_e32 v103, v103, v222
	s_waitcnt lgkmcnt(1)
	v_add_f32_e32 v120, v120, v225
	s_waitcnt lgkmcnt(0)
	v_add_f32_e32 v104, v104, v251
	v_add_f32_e32 v121, v121, v224
	v_add_f32_e32 v105, v105, v250
	s_nop 0
	v_add_u32_e32 v16, 0x1eabc, v247
	v_add_u32_e32 v222, 0x1ea3c, v247
	v_add_u32_e32 v224, 0x1eab4, v247
	v_add_u32_e32 v250, 0x1ea34, v247
	ds_read2_b32 v[16:17], v16 offset1:1
	ds_read2_b32 v[222:223], v222 offset1:1
	ds_read2_b32 v[224:225], v224 offset1:1
	ds_read2_b32 v[250:251], v250 offset1:1
	s_waitcnt lgkmcnt(3)
	v_add_f32_e32 v122, v122, v17
	s_waitcnt lgkmcnt(2)
	v_add_f32_e32 v106, v106, v223
	v_add_f32_e32 v123, v123, v16
	v_add_f32_e32 v107, v107, v222
	s_waitcnt lgkmcnt(1)
	v_add_f32_e32 v124, v124, v225
	s_waitcnt lgkmcnt(0)
	v_add_f32_e32 v108, v108, v251
	v_add_f32_e32 v125, v125, v224
	v_add_f32_e32 v109, v109, v250
	s_nop 0
	v_add_u32_e32 v16, 0x1ea9c, v247
	v_add_u32_e32 v222, 0x1ea1c, v247
	v_add_u32_e32 v224, 0x1ea94, v247
	ds_read2_b32 v[16:17], v16 offset1:1
	ds_read2_b32 v[222:223], v222 offset1:1
	ds_read2_b32 v[224:225], v224 offset1:1
	ds_read2_b32 v[250:251], v252 offset1:1
	s_waitcnt lgkmcnt(3)
	v_add_f32_e32 v126, v126, v17
	s_waitcnt lgkmcnt(2)
	v_add_f32_e32 v110, v110, v223
	v_add_f32_e32 v127, v127, v16
	v_add_f32_e32 v111, v111, v222
	s_waitcnt lgkmcnt(1)
	v_add_f32_e32 v128, v128, v225
	s_waitcnt lgkmcnt(0)
	v_add_f32_e32 v112, v112, v251
	v_add_f32_e32 v129, v129, v224
	v_add_f32_e32 v113, v113, v250
	s_nop 0

.LBB0_329:
	s_add_i32 s0, s86, 0x4000
	s_and_b32 s0, s0, 0xffff
	v_lshl_add_u64 v[16:17], v[224:225], 0, s[30:31]
	s_add_i32 s0, s0, s77
	s_mov_b32 m0, s0
	s_nop 0
	global_load_lds_dwordx4 v[16:17], off
	v_lshl_add_u64 v[16:17], v[222:223], 0, s[30:31]
	s_addk_i32 s0, 0x2000
	s_mov_b32 m0, s0
	s_nop 0
	global_load_lds_dwordx4 v[16:17], off
	s_add_i32 s75, s75, 5
	s_cmp_lt_i32 s75, 0
	s_branch .LBB0_305

.LBB0_901:
	s_add_i32 s75, s73, s81
	s_add_i32 s38, s75, 4
	s_cmp_lt_i32 s38, 0
.LBB0_903:
	s_cmp_lt_i32 s81, s72
	v_add_u32_e32 v247, v244, v245
	s_cbranch_scc1 .LBB0_905
	v_add_u32_e32 v166, 0x1ebfc, v247
	v_add_u32_e32 v168, 0x1eb7c, v247
	v_add_u32_e32 v174, 0x1ebf4, v247
	v_add_u32_e32 v176, 0x1eb74, v247
	ds_read2_b32 v[166:167], v166 offset1:1
	ds_read2_b32 v[168:169], v168 offset1:1
	ds_read2_b32 v[174:175], v174 offset1:1
	ds_read2_b32 v[176:177], v176 offset1:1
	s_waitcnt lgkmcnt(3)
	v_add_f32_e32 v114, v114, v167
	s_waitcnt lgkmcnt(2)
	v_add_f32_e32 v98, v98, v169
	v_add_f32_e32 v115, v115, v166
	v_add_f32_e32 v99, v99, v168
	s_waitcnt lgkmcnt(1)
	v_add_f32_e32 v116, v116, v175
	s_waitcnt lgkmcnt(0)
	v_add_f32_e32 v100, v100, v177
	v_add_f32_e32 v117, v117, v174
	v_add_f32_e32 v101, v101, v176
	v_add_u32_e32 v178, 0x1eb14, v247
	v_add_u32_e32 v166, 0x1ebdc, v247
	v_add_u32_e32 v168, 0x1eb5c, v247
	v_add_u32_e32 v174, 0x1ebd4, v247
	v_add_u32_e32 v176, 0x1eb54, v247
	ds_read2_b32 v[166:167], v166 offset1:1
	ds_read2_b32 v[168:169], v168 offset1:1
	ds_read2_b32 v[174:175], v174 offset1:1
	ds_read2_b32 v[176:177], v176 offset1:1
	s_waitcnt lgkmcnt(3)
	v_add_f32_e32 v118, v118, v167
	s_waitcnt lgkmcnt(2)
	v_add_f32_e32 v102, v102, v169
	v_add_f32_e32 v119, v119, v166
	v_add_f32_e32 v103, v103, v168
	s_waitcnt lgkmcnt(1)
	v_add_f32_e32 v120, v120, v175
	s_waitcnt lgkmcnt(0)
	v_add_f32_e32 v104, v104, v177
	v_add_f32_e32 v121, v121, v174
	v_add_f32_e32 v105, v105, v176
	s_nop 0
	v_add_u32_e32 v166, 0x1ebbc, v247
	v_add_u32_e32 v168, 0x1eb3c, v247
	v_add_u32_e32 v174, 0x1ebb4, v247
	v_add_u32_e32 v176, 0x1eb34, v247
	ds_read2_b32 v[166:167], v166 offset1:1
	ds_read2_b32 v[168:169], v168 offset1:1
	ds_read2_b32 v[174:175], v174 offset1:1
	ds_read2_b32 v[176:177], v176 offset1:1
	s_waitcnt lgkmcnt(3)
	v_add_f32_e32 v122, v122, v167
	s_waitcnt lgkmcnt(2)
	v_add_f32_e32 v106, v106, v169
	v_add_f32_e32 v123, v123, v166
	v_add_f32_e32 v107, v107, v168
	s_waitcnt lgkmcnt(1)
	v_add_f32_e32 v124, v124, v175
	s_waitcnt lgkmcnt(0)
	v_add_f32_e32 v108, v108, v177
	v_add_f32_e32 v125, v125, v174
	v_add_f32_e32 v109, v109, v176
	s_nop 0
	v_add_u32_e32 v166, 0x1eb9c, v247
	v_add_u32_e32 v168, 0x1eb1c, v247
	v_add_u32_e32 v174, 0x1eb94, v247
	ds_read2_b32 v[166:167], v166 offset1:1
	ds_read2_b32 v[168:169], v168 offset1:1
	ds_read2_b32 v[174:175], v174 offset1:1
	ds_read2_b32 v[176:177], v178 offset1:1
	s_waitcnt lgkmcnt(3)
	v_add_f32_e32 v126, v126, v167
	s_waitcnt lgkmcnt(2)
	v_add_f32_e32 v110, v110, v169
	v_add_f32_e32 v127, v127, v166
	v_add_f32_e32 v111, v111, v168
	s_waitcnt lgkmcnt(1)
	v_add_f32_e32 v128, v128, v175
	s_waitcnt lgkmcnt(0)
	v_add_f32_e32 v112, v112, v177
	v_add_f32_e32 v129, v129, v174
	v_add_f32_e32 v113, v113, v176
	s_nop 0

.LBB0_916:
	s_add_i32 s75, s75, 5
	s_cmp_lt_i32 s75, 0
.LBB0_918:
	s_add_i32 s0, s81, 1
	s_cmp_lt_i32 s0, s72
	s_cbranch_scc1 .LBB0_920
	v_add_u32_e32 v16, 0x1eafc, v247
	v_add_u32_e32 v222, 0x1ea7c, v247
	v_add_u32_e32 v224, 0x1eaf4, v247
	v_add_u32_e32 v250, 0x1ea74, v247
	ds_read2_b32 v[16:17], v16 offset1:1
	ds_read2_b32 v[222:223], v222 offset1:1
	ds_read2_b32 v[224:225], v224 offset1:1
	ds_read2_b32 v[250:251], v250 offset1:1
	s_waitcnt lgkmcnt(3)
	v_add_f32_e32 v114, v114, v17
	s_waitcnt lgkmcnt(2)
	v_add_f32_e32 v98, v98, v223
	v_add_f32_e32 v115, v115, v16
	v_add_f32_e32 v99, v99, v222
	s_waitcnt lgkmcnt(1)
	v_add_f32_e32 v116, v116, v225
	s_waitcnt lgkmcnt(0)
	v_add_f32_e32 v100, v100, v251
	v_add_f32_e32 v117, v117, v224
	v_add_f32_e32 v101, v101, v250
	v_add_u32_e32 v252, 0x1ea14, v247
	v_add_u32_e32 v16, 0x1eadc, v247
	v_add_u32_e32 v222, 0x1ea5c, v247
	v_add_u32_e32 v224, 0x1ead4, v247
	v_add_u32_e32 v250, 0x1ea54, v247
	ds_read2_b32 v[16:17], v16 offset1:1
	ds_read2_b32 v[222:223], v222 offset1:1
	ds_read2_b32 v[224:225], v224 offset1:1
	ds_read2_b32 v[250:251], v250 offset1:1
	s_waitcnt lgkmcnt(3)
	v_add_f32_e32 v118, v118, v17
	s_waitcnt lgkmcnt(2)
	v_add_f32_e32 v102, v102, v223
	v_add_f32_e32 v119, v119, v16
	v_add_f32_e32 v103, v103, v222
	s_waitcnt lgkmcnt(1)
	v_add_f32_e32 v120, v120, v225
	s_waitcnt lgkmcnt(0)
	v_add_f32_e32 v104, v104, v251
	v_add_f32_e32 v121, v121, v224
	v_add_f32_e32 v105, v105, v250
	s_nop 0
	v_add_u32_e32 v16, 0x1eabc, v247
	v_add_u32_e32 v222, 0x1ea3c, v247
	v_add_u32_e32 v224, 0x1eab4, v247
	v_add_u32_e32 v250, 0x1ea34, v247
	ds_read2_b32 v[16:17], v16 offset1:1
	ds_read2_b32 v[222:223], v222 offset1:1
	ds_read2_b32 v[224:225], v224 offset1:1
	ds_read2_b32 v[250:251], v250 offset1:1
	s_waitcnt lgkmcnt(3)
	v_add_f32_e32 v122, v122, v17
	s_waitcnt lgkmcnt(2)
	v_add_f32_e32 v106, v106, v223
	v_add_f32_e32 v123, v123, v16
	v_add_f32_e32 v107, v107, v222
	s_waitcnt lgkmcnt(1)
	v_add_f32_e32 v124, v124, v225
	s_waitcnt lgkmcnt(0)
	v_add_f32_e32 v108, v108, v251
	v_add_f32_e32 v125, v125, v224
	v_add_f32_e32 v109, v109, v250
	s_nop 0
	v_add_u32_e32 v16, 0x1ea9c, v247
	v_add_u32_e32 v222, 0x1ea1c, v247
	v_add_u32_e32 v224, 0x1ea94, v247
	ds_read2_b32 v[16:17], v16 offset1:1
	ds_read2_b32 v[222:223], v222 offset1:1
	ds_read2_b32 v[224:225], v224 offset1:1
	ds_read2_b32 v[250:251], v252 offset1:1
	s_waitcnt lgkmcnt(3)
	v_add_f32_e32 v126, v126, v17
	s_waitcnt lgkmcnt(2)
	v_add_f32_e32 v110, v110, v223
	v_add_f32_e32 v127, v127, v16
	v_add_f32_e32 v111, v111, v222
	s_waitcnt lgkmcnt(1)
	v_add_f32_e32 v128, v128, v225
	s_waitcnt lgkmcnt(0)
	v_add_f32_e32 v112, v112, v251
	v_add_f32_e32 v129, v129, v224
	v_add_f32_e32 v113, v113, v250
	s_nop 0

.LBB0_942:
	s_add_i32 s0, s80, 0x4000
	s_and_b32 s0, s0, 0xffff
	v_lshl_add_u64 v[16:17], v[224:225], 0, s[24:25]
	s_add_i32 s0, s0, s77
	s_mov_b32 m0, s0
	s_nop 0
	global_load_lds_dwordx4 v[16:17], off
	v_lshl_add_u64 v[16:17], v[222:223], 0, s[24:25]
	s_addk_i32 s0, 0x2000
	s_mov_b32 m0, s0
	s_nop 0
	global_load_lds_dwordx4 v[16:17], off
	s_add_i32 s75, s75, 5
	s_cmp_lt_i32 s75, 0
	s_branch .LBB0_918
